# edge staging loads with sc1 (L1 bypass) instead of plain; K3 CSR stores nt
# baseline (speedup 1.0000x reference)
_Z5k_hopILi0EEvPKiPK15HIP_vector_typeIiLj2EEPKS2_IjLj4EEPS6_S8_S8_PKfSB_Pf:
	s_lshr_b32 s3, s2, 3
	s_cmpk_gt_u32 s3, 156
	s_cbranch_scc1 .Lhq0_exit
	s_load_dwordx4 s[4:7], s[0:1], 0x0
	s_load_dwordx4 s[8:11], s[0:1], 0x10
	v_lshrrev_b32_e32 v2, 6, v0
	v_and_b32_e32 v3, 63, v0
	s_bfe_u32 s13, s2, 0x10002
	s_and_b32 s14, s2, 3
	v_readfirstlane_b32 s12, v2
	s_lshl_b32 s15, s3, 2
	s_add_i32 s15, s15, s12
	s_mul_i32 s15, s15, 40
	s_mul_i32 s16, s14, 25000
	s_add_i32 s15, s15, s16
	s_add_i32 s16, s16, 24960
	s_min_u32 s15, s15, s16
	s_mul_i32 s17, s13, 0x61a84
	s_waitcnt lgkmcnt(0)
	s_add_u32 s4, s4, s17
	s_addc_u32 s5, s5, 0
	s_mul_i32 s17, s13, 0x927c00
	s_add_u32 s6, s6, s17
	s_addc_u32 s7, s7, 0
	s_mul_i32 s17, s13, 0xc35000
	s_add_u32 s8, s8, s17
	s_addc_u32 s9, s9, 0
	s_add_u32 s10, s10, s17
	s_addc_u32 s11, s11, 0
	s_mul_i32 s28, s12, 6976
	s_mov_b32 s29, 0xffff80
	v_min_u32_e32 v4, 40, v3
	v_add_u32_e32 v4, s15, v4
	v_lshlrev_b32_e32 v4, 2, v4
	global_load_dword v5, v4, s[4:5]
	v_and_b32_e32 v1, 7, v0
	v_lshlrev_b32_e32 v1, 4, v1
	v_lshrrev_b32_e32 v2, 3, v3
	v_lshlrev_b32_e32 v2, 2, v2
	v_lshlrev_b32_e32 v4, 3, v3
	v_add_u32_e32 v6, s28, v4
	v_add_u32_e32 v7, 1, v3
	v_lshlrev_b32_e32 v7, 2, v7
	s_waitcnt vmcnt(0)
	v_readlane_b32 s18, v5, 0
	v_readlane_b32 s19, v5, 40
	ds_bpermute_b32 v8, v7, v5
	s_sub_i32 s20, s19, s18
	s_lshl_b32 s21, s18, 3
	s_add_u32 s22, s6, s21
	s_addc_u32 s23, s7, 0
	s_add_u32 s24, s22, 0x1000
	s_addc_u32 s25, s23, 0
	s_cmpk_gt_i32 s20, 832
	s_cbranch_scc1 .Lhq0_staged
	global_load_dwordx2 v[56:57], v4, s[22:23] offset:0 sc1
	s_cmpk_le_i32 s20, 64
	s_cbranch_scc1 .Lhq0_staged
	global_load_dwordx2 v[58:59], v4, s[22:23] offset:512 sc1
	s_cmpk_le_i32 s20, 128
	s_cbranch_scc1 .Lhq0_staged
	global_load_dwordx2 v[60:61], v4, s[22:23] offset:1024 sc1
	s_cmpk_le_i32 s20, 192
	s_cbranch_scc1 .Lhq0_staged
	global_load_dwordx2 v[62:63], v4, s[22:23] offset:1536 sc1
	s_cmpk_le_i32 s20, 256
	s_cbranch_scc1 .Lhq0_staged
	global_load_dwordx2 v[64:65], v4, s[22:23] offset:2048 sc1
	s_cmpk_le_i32 s20, 320
	s_cbranch_scc1 .Lhq0_staged
	global_load_dwordx2 v[66:67], v4, s[22:23] offset:2560 sc1
	s_cmpk_le_i32 s20, 384
	s_cbranch_scc1 .Lhq0_staged
	global_load_dwordx2 v[68:69], v4, s[22:23] offset:3072 sc1
	s_cmpk_le_i32 s20, 448
	s_cbranch_scc1 .Lhq0_staged
	global_load_dwordx2 v[70:71], v4, s[22:23] offset:3584 sc1
	s_cmpk_le_i32 s20, 512
	s_cbranch_scc1 .Lhq0_staged
	global_load_dwordx2 v[72:73], v4, s[24:25] offset:0 sc1
	s_cmpk_le_i32 s20, 576
	s_cbranch_scc1 .Lhq0_staged
	global_load_dwordx2 v[74:75], v4, s[24:25] offset:512 sc1
	s_cmpk_le_i32 s20, 640
	s_cbranch_scc1 .Lhq0_staged
	global_load_dwordx2 v[76:77], v4, s[24:25] offset:1024 sc1
	s_cmpk_le_i32 s20, 704
	s_cbranch_scc1 .Lhq0_staged
	global_load_dwordx2 v[78:79], v4, s[24:25] offset:1536 sc1
	s_cmpk_le_i32 s20, 768
	s_cbranch_scc1 .Lhq0_staged
	global_load_dwordx2 v[80:81], v4, s[24:25] offset:2048 sc1

_Z5k_hopILi1EEvPKiPK15HIP_vector_typeIiLj2EEPKS2_IjLj4EEPS6_S8_S8_PKfSB_Pf:
	s_lshr_b32 s3, s2, 3
	s_cmpk_gt_u32 s3, 156
	s_cbranch_scc1 .Lhq1_exit
	s_load_dwordx4 s[4:7], s[0:1], 0x0
	s_load_dwordx4 s[8:11], s[0:1], 0x10
	s_load_dwordx4 s[48:51], s[0:1], 0x20
	s_load_dwordx4 s[52:55], s[0:1], 0x30
	s_load_dwordx2 s[56:57], s[0:1], 0x40
	v_lshrrev_b32_e32 v2, 6, v0
	v_and_b32_e32 v3, 63, v0
	s_bfe_u32 s13, s2, 0x10002
	s_and_b32 s14, s2, 3
	v_readfirstlane_b32 s12, v2
	s_lshl_b32 s15, s3, 2
	s_add_i32 s15, s15, s12
	s_mul_i32 s15, s15, 40
	s_mul_i32 s16, s14, 25000
	s_add_i32 s15, s15, s16
	s_add_i32 s16, s16, 24960
	s_min_u32 s15, s15, s16
	s_mul_i32 s17, s13, 0x61a84
	s_waitcnt lgkmcnt(0)
	s_add_u32 s4, s4, s17
	s_addc_u32 s5, s5, 0
	s_mul_i32 s17, s13, 0x927c00
	s_add_u32 s6, s6, s17
	s_addc_u32 s7, s7, 0
	s_mul_i32 s17, s13, 0xc35000
	s_add_u32 s8, s8, s17
	s_addc_u32 s9, s9, 0
	s_add_u32 s48, s48, s17
	s_addc_u32 s49, s49, 0
	s_add_u32 s50, s50, s17
	s_addc_u32 s51, s51, 0
	s_cmp_eq_u32 s13, 0
	s_cselect_b32 s58, s52, s54
	s_cselect_b32 s59, s53, s55
	s_load_dwordx4 s[52:55], s[58:59], 0x0
	s_lshl_b32 s17, s13, 8
	s_add_u32 s56, s56, s17
	s_addc_u32 s57, s57, 0
	s_mul_i32 s28, s12, 6976
	s_mov_b32 s29, 0xffff80
	v_min_u32_e32 v4, 40, v3
	v_add_u32_e32 v4, s15, v4
	v_lshlrev_b32_e32 v4, 2, v4
	global_load_dword v5, v4, s[4:5]
	v_and_b32_e32 v1, 7, v0
	v_lshlrev_b32_e32 v1, 4, v1
	v_lshrrev_b32_e32 v2, 3, v3
	v_lshlrev_b32_e32 v2, 2, v2
	v_lshlrev_b32_e32 v4, 3, v3
	v_add_u32_e32 v6, s28, v4
	v_add_u32_e32 v7, 1, v3
	v_lshlrev_b32_e32 v7, 2, v7
	s_waitcnt vmcnt(0)
	v_readlane_b32 s18, v5, 0
	v_readlane_b32 s19, v5, 40
	ds_bpermute_b32 v8, v7, v5
	s_sub_i32 s20, s19, s18
	s_lshl_b32 s21, s18, 3
	s_add_u32 s22, s6, s21
	s_addc_u32 s23, s7, 0
	s_add_u32 s24, s22, 0x1000
	s_addc_u32 s25, s23, 0
	s_cmpk_gt_i32 s20, 832
	s_cbranch_scc1 .Lhq1_staged
	global_load_dwordx2 v[56:57], v4, s[22:23] offset:0 sc1
	s_cmpk_le_i32 s20, 64
	s_cbranch_scc1 .Lhq1_staged
	global_load_dwordx2 v[58:59], v4, s[22:23] offset:512 sc1
	s_cmpk_le_i32 s20, 128
	s_cbranch_scc1 .Lhq1_staged
	global_load_dwordx2 v[60:61], v4, s[22:23] offset:1024 sc1
	s_cmpk_le_i32 s20, 192
	s_cbranch_scc1 .Lhq1_staged
	global_load_dwordx2 v[62:63], v4, s[22:23] offset:1536 sc1
	s_cmpk_le_i32 s20, 256
	s_cbranch_scc1 .Lhq1_staged
	global_load_dwordx2 v[64:65], v4, s[22:23] offset:2048 sc1
	s_cmpk_le_i32 s20, 320
	s_cbranch_scc1 .Lhq1_staged
	global_load_dwordx2 v[66:67], v4, s[22:23] offset:2560 sc1
	s_cmpk_le_i32 s20, 384
	s_cbranch_scc1 .Lhq1_staged
	global_load_dwordx2 v[68:69], v4, s[22:23] offset:3072 sc1
	s_cmpk_le_i32 s20, 448
	s_cbranch_scc1 .Lhq1_staged
	global_load_dwordx2 v[70:71], v4, s[22:23] offset:3584 sc1
	s_cmpk_le_i32 s20, 512
	s_cbranch_scc1 .Lhq1_staged
	global_load_dwordx2 v[72:73], v4, s[24:25] offset:0 sc1
	s_cmpk_le_i32 s20, 576
	s_cbranch_scc1 .Lhq1_staged
	global_load_dwordx2 v[74:75], v4, s[24:25] offset:512 sc1
	s_cmpk_le_i32 s20, 640
	s_cbranch_scc1 .Lhq1_staged
	global_load_dwordx2 v[76:77], v4, s[24:25] offset:1024 sc1
	s_cmpk_le_i32 s20, 704
	s_cbranch_scc1 .Lhq1_staged
	global_load_dwordx2 v[78:79], v4, s[24:25] offset:1536 sc1
	s_cmpk_le_i32 s20, 768
	s_cbranch_scc1 .Lhq1_staged
	global_load_dwordx2 v[80:81], v4, s[24:25] offset:2048 sc1
